# y phase: 24 transpose-read addresses from 4 base registers + immediate offsets (51 fewer VALU ahead of the y MFMAs)
# speedup vs baseline: 1.0249x; 1.0249x over previous
.LBB1_4:
	s_or_b64 exec, exec, s[4:5]
	v_lshl_or_b32 v4, v27, 1, v96
	v_lshl_or_b32 v3, v4, 7, v3
	v_or_b32_e32 v5, 0x23600, v3
	v_or_b32_e32 v3, 0x23640, v3
	s_waitcnt lgkmcnt(0)
	s_barrier
	ds_read_b32 v5, v5
	ds_read_b32 v3, v3
	v_lshrrev_b32_e32 v216, 5, v126
	v_and_b32_e32 v217, 3, v216
	v_lshrrev_b32_e32 v216, 2, v216
	v_and_b32_e32 v216, 1, v216
	v_mul_u32_u24_e32 v216, 0x60, v216
	v_lshl_add_u32 v216, v119, 3, v216
	v_bfe_u32 v218, v116, 2, 2
	v_add_u32_e32 v216, v216, v218
	v_lshlrev_b32_e32 v216, 8, v216
	v_lshrrev_b32_e32 v219, 1, v217
	v_mul_u32_u24_e32 v219, 0xc000, v219
	v_add_u32_e32 v216, v216, v219
	v_and_b32_e32 v217, 1, v217
	v_lshlrev_b32_e32 v217, 3, v217
	v_bfe_u32 v219, v116, 4, 1
	v_lshl_or_b32 v217, v219, 1, v217
	v_bfe_u32 v219, v116, 1, 1
	v_or_b32_e32 v217, v217, v219
	v_lshlrev_b32_e32 v218, 2, v218
	v_lshl_or_b32 v218, v119, 1, v218
	v_xor_b32_e32 v217, v217, v218
	v_lshl_or_b32 v216, v217, 4, v216
	v_and_b32_e32 v217, 1, v116
	v_lshl_or_b32 v212, v217, 3, v216
	v_xor_b32_e32 v213, 16, v212
	v_add_u32_e32 v213, 0x400, v213
	v_xor_b32_e32 v214, 64, v212
	v_xor_b32_e32 v215, 64, v213
	v_mad_u32_u24 v4, v4, s7, v13
	v_lshl_add_u32 v4, v119, 4, v4
	v_or_b32_e32 v6, 0x20000, v4
	ds_read_b128 v[16:19], v6
	s_waitcnt lgkmcnt(1)
	v_add_f32_e32 v3, v5, v3
	v_add_u32_e32 v5, 0x20020, v4
	v_add_u32_e32 v6, 0x20040, v4
	ds_read_b128 v[112:115], v5
	ds_read_b128 v[108:111], v6
	v_add_u32_e32 v5, 0x20060, v4
	v_add_u32_e32 v6, 0x20080, v4
	ds_read_b128 v[104:107], v5
	ds_read_b128 v[96:99], v6
	v_and_b32_e32 v164, 8, v121
	v_add_u32_e32 v4, 0x200a0, v4
	ds_read_b128 v[100:103], v4
	ds_read_b64_tr_b16 v[4:5], v212
	ds_read_b64_tr_b16 v[6:7], v213
	ds_read_b64_tr_b16 v[20:21], v212 offset:4096
	ds_read_b64_tr_b16 v[22:23], v213 offset:4096
	ds_read_b64_tr_b16 v[28:29], v212 offset:8192
	ds_read_b64_tr_b16 v[30:31], v213 offset:8192
	ds_read_b64_tr_b16 v[128:129], v212 offset:12288
	ds_read_b64_tr_b16 v[130:131], v213 offset:12288
	ds_read_b64_tr_b16 v[132:133], v212 offset:16384
	ds_read_b64_tr_b16 v[134:135], v213 offset:16384
	ds_read_b64_tr_b16 v[136:137], v212 offset:20480
	ds_read_b64_tr_b16 v[138:139], v213 offset:20480
	ds_read_b64_tr_b16 v[140:141], v214
	ds_read_b64_tr_b16 v[142:143], v215
	ds_read_b64_tr_b16 v[144:145], v214 offset:4096
	ds_read_b64_tr_b16 v[146:147], v215 offset:4096
	ds_read_b64_tr_b16 v[148:149], v214 offset:8192
	ds_read_b64_tr_b16 v[150:151], v215 offset:8192
	ds_read_b64_tr_b16 v[152:153], v214 offset:12288
	ds_read_b64_tr_b16 v[154:155], v215 offset:12288
	ds_read_b64_tr_b16 v[156:157], v214 offset:16384
	v_div_scale_f32 v1, s[8:9], v3, v3, 1.0
	v_rcp_f32_e32 v9, v1
	ds_read_b64_tr_b16 v[158:159], v215 offset:16384
	ds_read_b64_tr_b16 v[160:161], v214 offset:20480
	ds_read_b64_tr_b16 v[162:163], v215 offset:20480
	s_mov_b32 s4, 0xc000
	s_movk_i32 s5, 0x4000
	v_fma_f32 v0, -v1, v9, 1.0
	v_fmac_f32_e32 v9, v0, v9
	v_div_scale_f32 v0, vcc, 1.0, v3, 1.0
	v_mul_f32_e32 v2, v0, v9
	v_fma_f32 v8, -v1, v2, v0
	v_fmac_f32_e32 v2, v8, v9
	v_fma_f32 v0, -v1, v2, v0
	v_div_fmas_f32 v0, v0, v9, v2
	v_div_fixup_f32 v124, v0, v3, 1.0
	s_waitcnt lgkmcnt(14)
	v_mfma_f32_32x32x16_f16 v[0:15], v[4:7], v[16:19], 0
	s_mov_b32 s7, 0x18000
	v_lshlrev_b32_e32 v172, 2, v126
	v_mov_b32_e32 v173, 0
	v_mfma_f32_32x32x16_f16 v[0:15], v[20:23], v[112:115], v[0:15]
	v_or_b32_e32 v20, v26, v116
	v_and_b32_e32 v21, 0x4000, v118
	v_lshl_or_b32 v20, v20, 8, v21
	v_bitop3_b32 v118, v121, v120, 8 bitop3:0x6c
	v_or3_b32 v121, v20, v125, s7
	v_mfma_f32_32x32x16_f16 v[0:15], v[28:31], v[108:111], v[0:15]
	v_mfma_f32_32x32x16_f16 v[0:15], v[128:131], v[104:107], v[0:15]
	v_mfma_f32_32x32x16_f16 v[0:15], v[132:135], v[96:99], v[0:15]
	s_waitcnt lgkmcnt(12)
	v_mfma_f32_32x32x16_f16 v[0:15], v[136:139], v[100:103], v[0:15]
	s_nop 11
	v_fma_mixlo_f16 v20, v124, v0, 0
	v_mov_b32_e32 v0, v1
	v_mov_b32_e32 v1, v2
	v_pk_mul_f32 v[0:1], v[124:125], v[0:1] op_sel_hi:[0,1]
	v_cvt_pk_f16_f32 v1, v0, v1
	v_pack_b32_f16 v0, v20, v1
	s_waitcnt lgkmcnt(10)
	v_mfma_f32_32x32x16_f16 v[16:31], v[140:143], v[16:19], 0
	v_fma_mixlo_f16 v2, v124, v3, 0
	v_alignbit_b32 v1, v2, v1, 16
	v_lshl_or_b32 v2, v118, 4, v121
	ds_write_b64 v2, v[0:1]
	v_mov_b32_e32 v0, v5
	v_mov_b32_e32 v1, v6
	v_pk_mul_f32 v[0:1], v[124:125], v[0:1] op_sel_hi:[0,1]
	s_waitcnt lgkmcnt(9)
	v_mfma_f32_32x32x16_f16 v[16:31], v[144:147], v[112:115], v[16:31]
	v_fma_mixlo_f16 v2, v124, v4, 0
	v_cvt_pk_f16_f32 v1, v0, v1
	v_pack_b32_f16 v0, v2, v1
	v_fma_mixlo_f16 v2, v124, v7, 0
	v_alignbit_b32 v1, v2, v1, 16
	v_bitop3_b32 v2, v164, v120, 1 bitop3:0x36
	v_lshl_or_b32 v2, v2, 4, v121
	s_waitcnt lgkmcnt(7)
	v_mfma_f32_32x32x16_f16 v[16:31], v[148:151], v[108:111], v[16:31]
	ds_write_b64 v2, v[0:1]
	v_mov_b32_e32 v0, v9
	v_mov_b32_e32 v1, v10
	v_mul_f32_e64 v0, v124, v0
	v_mul_f32_e64 v1, v124, v1
	v_fma_mixlo_f16 v2, v124, v8, 0
	v_cvt_pk_f16_f32 v1, v0, v1
	v_pack_b32_f16 v0, v2, v1
	s_waitcnt lgkmcnt(6)
	v_mfma_f32_32x32x16_f16 v[16:31], v[152:155], v[104:107], v[16:31]
	v_fma_mixlo_f16 v2, v124, v11, 0
	v_alignbit_b32 v1, v2, v1, 16
	v_bitop3_b32 v2, v164, v120, 2 bitop3:0x36
	v_lshl_or_b32 v2, v2, 4, v121
	ds_write_b64 v2, v[0:1]
	v_mov_b32_e32 v0, v13
	v_mov_b32_e32 v1, v14
	s_waitcnt lgkmcnt(5)
	v_mfma_f32_32x32x16_f16 v[16:31], v[156:159], v[96:99], v[16:31]
	v_mul_f32_e64 v0, v124, v0
	v_mul_f32_e64 v1, v124, v1
	v_fma_mixlo_f16 v2, v124, v12, 0
	v_cvt_pk_f16_f32 v1, v0, v1
	v_pack_b32_f16 v0, v2, v1
	v_fma_mixlo_f16 v2, v124, v15, 0
	v_alignbit_b32 v1, v2, v1, 16
	v_bitop3_b32 v2, v164, v120, 3 bitop3:0x36
	s_waitcnt lgkmcnt(3)
	v_mfma_f32_32x32x16_f16 v[16:31], v[160:163], v[100:103], v[16:31]
	v_lshl_or_b32 v2, v2, 4, v121
	ds_write_b64 v2, v[0:1]
	s_nop 9
	v_mov_b32_e32 v0, v17
	v_mov_b32_e32 v1, v18
	v_pk_mul_f32 v[0:1], v[124:125], v[0:1] op_sel_hi:[0,1]
	v_fma_mixlo_f16 v2, v124, v16, 0
	v_cvt_pk_f16_f32 v1, v0, v1
	v_pack_b32_f16 v0, v2, v1
	v_fma_mixlo_f16 v2, v124, v19, 0
	v_alignbit_b32 v1, v2, v1, 16
	v_bitop3_b32 v2, v164, v120, 4 bitop3:0x36
	v_lshl_or_b32 v2, v2, 4, v121
	ds_write_b64 v2, v[0:1]
	v_mov_b32_e32 v0, v21
	v_mov_b32_e32 v1, v22
	v_pk_mul_f32 v[0:1], v[124:125], v[0:1] op_sel_hi:[0,1]
	v_fma_mixlo_f16 v2, v124, v20, 0
	v_cvt_pk_f16_f32 v1, v0, v1
	v_pack_b32_f16 v0, v2, v1
	v_fma_mixlo_f16 v2, v124, v23, 0
	v_alignbit_b32 v1, v2, v1, 16
	v_bitop3_b32 v2, v164, v120, 5 bitop3:0x36
	v_lshl_or_b32 v2, v2, 4, v121
	ds_write_b64 v2, v[0:1]
	v_mov_b32_e32 v0, v25
	v_mov_b32_e32 v1, v26
	v_pk_mul_f32 v[0:1], v[124:125], v[0:1] op_sel_hi:[0,1]
	v_fma_mixlo_f16 v2, v124, v24, 0
	v_cvt_pk_f16_f32 v1, v0, v1
	v_pack_b32_f16 v0, v2, v1
	v_fma_mixlo_f16 v2, v124, v27, 0
	v_alignbit_b32 v1, v2, v1, 16
	v_bitop3_b32 v2, v164, v120, 6 bitop3:0x36
	v_lshl_or_b32 v2, v2, 4, v121
	ds_write_b64 v2, v[0:1]
	v_mov_b32_e32 v0, v29
	v_mov_b32_e32 v1, v30
	v_pk_mul_f32 v[0:1], v[124:125], v[0:1] op_sel_hi:[0,1]
	v_fma_mixlo_f16 v2, v124, v28, 0
	v_cvt_pk_f16_f32 v1, v0, v1
	v_pack_b32_f16 v0, v2, v1
	v_fma_mixlo_f16 v2, v124, v31, 0
	v_alignbit_b32 v1, v2, v1, 16
	v_bitop3_b32 v2, v164, v120, 7 bitop3:0x36
	v_lshl_or_b32 v2, v2, 4, v121
	ds_write_b64 v2, v[0:1]
	v_lshl_add_u64 v[0:1], s[0:1], 0, v[172:173]
	v_lshlrev_b32_e32 v172, 2, v127
	v_lshl_add_u64 v[0:1], v[0:1], 0, v[172:173]
	s_waitcnt lgkmcnt(0)
	s_barrier
	v_and_b32_e32 v245, 15, v116
	v_lshrrev_b32_e32 v246, 4, v116
	v_lshl_or_b32 v246, v119, 1, v246
	v_lshrrev_b32_e32 v250, 5, v126
	v_and_b32_e32 v250, 7, v250
	v_and_b32_e32 v247, 1, v246
	v_lshrrev_b32_e32 v248, 1, v246
	v_xor_b32_e32 v248, v248, v247
	v_lshl_or_b32 v247, v247, 1, v248
	v_and_b32_e32 v248, 3, v245
	v_lshrrev_b32_e32 v249, 2, v245
	v_lshl_or_b32 v248, v248, 2, v249
	v_xor_b32_e32 v247, v247, v248
	v_lshlrev_b32_e32 v240, 8, v245
	v_lshl_or_b32 v240, v247, 4, v240
	v_add_u32_e32 v240, 0x18000, v240
	v_xor_b32_e32 v241, 64, v240
	v_xor_b32_e32 v242, 0x80, v240
	v_xor_b32_e32 v243, 0xc0, v240
	v_lshlrev_b32_e32 v249, 7, v250
	v_lshl_or_b32 v249, v246, 4, v249
	v_and_b32_e32 v249, 0x3f0, v249
	global_load_dwordx4 v[96:99], v249, s[34:35]
	global_load_dwordx4 v[100:103], v249, s[34:35] offset:64
	v_lshlrev_b32_e32 v244, 19, v250
	v_lshl_or_b32 v244, v246, 16, v244
	v_lshl_or_b32 v244, v245, 3, v244
	v_and_b32_e32 v244, 0x3fff78, v244
	s_lshl_b64 s[22:23], s[2:3], 22
	s_add_u32 s22, s22, s30
	s_addc_u32 s23, s23, s31
	s_lshl_b32 s24, s14, 3
	s_add_u32 s22, s22, s24
	s_addc_u32 s23, s23, 0
	ds_read_b128 v[112:115], v240
	ds_read_b128 v[144:147], v240 offset:8192
	ds_read_b128 v[116:119], v241
	ds_read_b128 v[148:151], v241 offset:8192
	ds_read_b128 v[120:123], v242
	ds_read_b128 v[152:155], v242 offset:8192
	ds_read_b128 v[124:127], v243
	ds_read_b128 v[156:159], v243 offset:8192
	ds_read_b128 v[128:131], v240 offset:16384
	ds_read_b128 v[160:163], v240 offset:24576
	ds_read_b128 v[132:135], v241 offset:16384
	ds_read_b128 v[164:167], v241 offset:24576
	ds_read_b128 v[136:139], v242 offset:16384
	ds_read_b128 v[168:171], v242 offset:24576
	ds_read_b128 v[140:143], v243 offset:16384
	ds_read_b128 v[172:175], v243 offset:24576
	s_waitcnt vmcnt(2)
	s_waitcnt lgkmcnt(14)
	v_mfma_f32_16x16x32_f16 v[0:3], v[36:39], v[112:115], 0
	v_mfma_f32_16x16x32_f16 v[4:7], v[36:39], v[144:147], 0
	v_mfma_f32_16x16x32_f16 v[8:11], v[76:79], v[112:115], 0
	v_mfma_f32_16x16x32_f16 v[12:15], v[76:79], v[144:147], 0
	s_waitcnt lgkmcnt(12)
	v_mfma_f32_16x16x32_f16 v[0:3], v[32:35], v[116:119], v[0:3]
	v_mfma_f32_16x16x32_f16 v[4:7], v[32:35], v[148:151], v[4:7]
	v_mfma_f32_16x16x32_f16 v[8:11], v[72:75], v[116:119], v[8:11]
	v_mfma_f32_16x16x32_f16 v[12:15], v[72:75], v[148:151], v[12:15]
	s_waitcnt lgkmcnt(10)
	v_mfma_f32_16x16x32_f16 v[0:3], v[64:67], v[120:123], v[0:3]
	v_mfma_f32_16x16x32_f16 v[4:7], v[64:67], v[152:155], v[4:7]
	v_mfma_f32_16x16x32_f16 v[8:11], v[68:71], v[120:123], v[8:11]
	v_mfma_f32_16x16x32_f16 v[12:15], v[68:71], v[152:155], v[12:15]
	s_waitcnt lgkmcnt(8)
	v_mfma_f32_16x16x32_f16 v[0:3], v[48:51], v[124:127], v[0:3]
	v_mfma_f32_16x16x32_f16 v[4:7], v[48:51], v[156:159], v[4:7]
	v_mfma_f32_16x16x32_f16 v[8:11], v[52:55], v[124:127], v[8:11]
	v_mfma_f32_16x16x32_f16 v[12:15], v[52:55], v[156:159], v[12:15]
	s_waitcnt lgkmcnt(6)
	v_mfma_f32_16x16x32_f16 v[0:3], v[92:95], v[128:131], v[0:3]
	v_mfma_f32_16x16x32_f16 v[4:7], v[92:95], v[160:163], v[4:7]
	v_mfma_f32_16x16x32_f16 v[8:11], v[60:63], v[128:131], v[8:11]
	v_mfma_f32_16x16x32_f16 v[12:15], v[60:63], v[160:163], v[12:15]
	s_waitcnt lgkmcnt(4)
	v_mfma_f32_16x16x32_f16 v[0:3], v[84:87], v[132:135], v[0:3]
	v_mfma_f32_16x16x32_f16 v[4:7], v[84:87], v[164:167], v[4:7]
	v_mfma_f32_16x16x32_f16 v[8:11], v[56:59], v[132:135], v[8:11]
	v_mfma_f32_16x16x32_f16 v[12:15], v[56:59], v[164:167], v[12:15]
	s_waitcnt lgkmcnt(2)
	v_mfma_f32_16x16x32_f16 v[0:3], v[80:83], v[136:139], v[0:3]
	v_mfma_f32_16x16x32_f16 v[4:7], v[80:83], v[168:171], v[4:7]
	v_mfma_f32_16x16x32_f16 v[8:11], v[44:47], v[136:139], v[8:11]
	v_mfma_f32_16x16x32_f16 v[12:15], v[44:47], v[168:171], v[12:15]
	s_waitcnt lgkmcnt(0)
	v_mfma_f32_16x16x32_f16 v[0:3], v[88:91], v[140:143], v[0:3]
	v_mfma_f32_16x16x32_f16 v[4:7], v[88:91], v[172:175], v[4:7]
	v_mfma_f32_16x16x32_f16 v[8:11], v[40:43], v[140:143], v[8:11]
	v_mfma_f32_16x16x32_f16 v[12:15], v[40:43], v[172:175], v[12:15]
	ds_read_b128 v[176:179], v240 offset:4096
	ds_read_b128 v[208:211], v240 offset:12288
	ds_read_b128 v[180:183], v241 offset:4096
	ds_read_b128 v[212:215], v241 offset:12288
	ds_read_b128 v[184:187], v242 offset:4096
	ds_read_b128 v[216:219], v242 offset:12288
	ds_read_b128 v[188:191], v243 offset:4096
	ds_read_b128 v[220:223], v243 offset:12288
	ds_read_b128 v[192:195], v240 offset:20480
	ds_read_b128 v[224:227], v240 offset:28672
	ds_read_b128 v[196:199], v241 offset:20480
	ds_read_b128 v[228:231], v241 offset:28672
	ds_read_b128 v[200:203], v242 offset:20480
	ds_read_b128 v[232:235], v242 offset:28672
	ds_read_b128 v[204:207], v243 offset:20480
	ds_read_b128 v[236:239], v243 offset:28672
	s_waitcnt vmcnt(0)
	s_waitcnt lgkmcnt(14)
	v_mfma_f32_16x16x32_f16 v[16:19], v[36:39], v[176:179], 0
	v_mfma_f32_16x16x32_f16 v[20:23], v[36:39], v[208:211], 0
	v_mfma_f32_16x16x32_f16 v[24:27], v[76:79], v[176:179], 0
	v_mfma_f32_16x16x32_f16 v[28:31], v[76:79], v[208:211], 0
	s_add_u32 s26, s22, 0x0
	s_addc_u32 s27, s23, 0
	v_add_f32_e32 v104, v0, v96
	v_add_f32_e32 v105, v4, v96
	global_store_dwordx2 v244, v[104:105], s[26:27] nt
	s_waitcnt lgkmcnt(12)
	v_mfma_f32_16x16x32_f16 v[16:19], v[32:35], v[180:183], v[16:19]
	v_mfma_f32_16x16x32_f16 v[20:23], v[32:35], v[212:215], v[20:23]
	v_mfma_f32_16x16x32_f16 v[24:27], v[72:75], v[180:183], v[24:27]
	v_mfma_f32_16x16x32_f16 v[28:31], v[72:75], v[212:215], v[28:31]
	s_add_u32 s26, s22, 0x4000
	s_addc_u32 s27, s23, 0
	v_add_f32_e32 v106, v1, v97
	v_add_f32_e32 v107, v5, v97
	global_store_dwordx2 v244, v[106:107], s[26:27] nt
	s_waitcnt lgkmcnt(10)
	v_mfma_f32_16x16x32_f16 v[16:19], v[64:67], v[184:187], v[16:19]
	v_mfma_f32_16x16x32_f16 v[20:23], v[64:67], v[216:219], v[20:23]
	v_mfma_f32_16x16x32_f16 v[24:27], v[68:71], v[184:187], v[24:27]
	v_mfma_f32_16x16x32_f16 v[28:31], v[68:71], v[216:219], v[28:31]
	s_add_u32 s26, s22, 0x8000
	s_addc_u32 s27, s23, 0
	v_add_f32_e32 v108, v2, v98
	v_add_f32_e32 v109, v6, v98
	global_store_dwordx2 v244, v[108:109], s[26:27] nt
	s_waitcnt lgkmcnt(8)
	v_mfma_f32_16x16x32_f16 v[16:19], v[48:51], v[188:191], v[16:19]
	v_mfma_f32_16x16x32_f16 v[20:23], v[48:51], v[220:223], v[20:23]
	v_mfma_f32_16x16x32_f16 v[24:27], v[52:55], v[188:191], v[24:27]
	v_mfma_f32_16x16x32_f16 v[28:31], v[52:55], v[220:223], v[28:31]
	s_add_u32 s26, s22, 0xc000
	s_addc_u32 s27, s23, 0
	v_add_f32_e32 v110, v3, v99
	v_add_f32_e32 v111, v7, v99
	global_store_dwordx2 v244, v[110:111], s[26:27] nt
	s_waitcnt lgkmcnt(6)
	v_mfma_f32_16x16x32_f16 v[16:19], v[92:95], v[192:195], v[16:19]
	v_mfma_f32_16x16x32_f16 v[20:23], v[92:95], v[224:227], v[20:23]
	v_mfma_f32_16x16x32_f16 v[24:27], v[60:63], v[192:195], v[24:27]
	v_mfma_f32_16x16x32_f16 v[28:31], v[60:63], v[224:227], v[28:31]
	s_add_u32 s26, s22, 0x40000
	s_addc_u32 s27, s23, 0
	v_add_f32_e32 v104, v8, v100
	v_add_f32_e32 v105, v12, v100
	global_store_dwordx2 v244, v[104:105], s[26:27] nt
	s_waitcnt lgkmcnt(4)
	v_mfma_f32_16x16x32_f16 v[16:19], v[84:87], v[196:199], v[16:19]
	v_mfma_f32_16x16x32_f16 v[20:23], v[84:87], v[228:231], v[20:23]
	v_mfma_f32_16x16x32_f16 v[24:27], v[56:59], v[196:199], v[24:27]
	v_mfma_f32_16x16x32_f16 v[28:31], v[56:59], v[228:231], v[28:31]
	s_add_u32 s26, s22, 0x44000
	s_addc_u32 s27, s23, 0
	v_add_f32_e32 v106, v9, v101
	v_add_f32_e32 v107, v13, v101
	global_store_dwordx2 v244, v[106:107], s[26:27] nt
	s_waitcnt lgkmcnt(2)
	v_mfma_f32_16x16x32_f16 v[16:19], v[80:83], v[200:203], v[16:19]
	v_mfma_f32_16x16x32_f16 v[20:23], v[80:83], v[232:235], v[20:23]
	v_mfma_f32_16x16x32_f16 v[24:27], v[44:47], v[200:203], v[24:27]
	v_mfma_f32_16x16x32_f16 v[28:31], v[44:47], v[232:235], v[28:31]
	s_add_u32 s26, s22, 0x48000
	s_addc_u32 s27, s23, 0
	v_add_f32_e32 v108, v10, v102
	v_add_f32_e32 v109, v14, v102
	global_store_dwordx2 v244, v[108:109], s[26:27] nt
	s_waitcnt lgkmcnt(0)
	v_mfma_f32_16x16x32_f16 v[16:19], v[88:91], v[204:207], v[16:19]
	v_mfma_f32_16x16x32_f16 v[20:23], v[88:91], v[236:239], v[20:23]
	v_mfma_f32_16x16x32_f16 v[24:27], v[40:43], v[204:207], v[24:27]
	v_mfma_f32_16x16x32_f16 v[28:31], v[40:43], v[236:239], v[28:31]
	s_add_u32 s26, s22, 0x4c000
	s_addc_u32 s27, s23, 0
	v_add_f32_e32 v110, v11, v103
	v_add_f32_e32 v111, v15, v103
	global_store_dwordx2 v244, v[110:111], s[26:27] nt
	s_nop 7
	s_nop 1
	s_add_u32 s26, s22, 0x0
	s_addc_u32 s27, s23, 0
	v_add_f32_e32 v104, v16, v96
	v_add_f32_e32 v105, v20, v96
	global_store_dwordx2 v244, v[104:105], s[26:27] offset:128 nt
	s_add_u32 s26, s22, 0x4000
	s_addc_u32 s27, s23, 0
	v_add_f32_e32 v106, v17, v97
	v_add_f32_e32 v107, v21, v97
	global_store_dwordx2 v244, v[106:107], s[26:27] offset:128 nt
	s_add_u32 s26, s22, 0x8000
	s_addc_u32 s27, s23, 0
	v_add_f32_e32 v108, v18, v98
	v_add_f32_e32 v109, v22, v98
	global_store_dwordx2 v244, v[108:109], s[26:27] offset:128 nt
	s_add_u32 s26, s22, 0xc000
	s_addc_u32 s27, s23, 0
	v_add_f32_e32 v110, v19, v99
	v_add_f32_e32 v111, v23, v99
	global_store_dwordx2 v244, v[110:111], s[26:27] offset:128 nt
	s_add_u32 s26, s22, 0x40000
	s_addc_u32 s27, s23, 0
	v_add_f32_e32 v104, v24, v100
	v_add_f32_e32 v105, v28, v100
	global_store_dwordx2 v244, v[104:105], s[26:27] offset:128 nt
	s_add_u32 s26, s22, 0x44000
	s_addc_u32 s27, s23, 0
	v_add_f32_e32 v106, v25, v101
	v_add_f32_e32 v107, v29, v101
	global_store_dwordx2 v244, v[106:107], s[26:27] offset:128 nt
	s_add_u32 s26, s22, 0x48000
	s_addc_u32 s27, s23, 0
	v_add_f32_e32 v108, v26, v102
	v_add_f32_e32 v109, v30, v102
	global_store_dwordx2 v244, v[108:109], s[26:27] offset:128 nt
	s_add_u32 s26, s22, 0x4c000
	s_addc_u32 s27, s23, 0
	v_add_f32_e32 v110, v27, v103
	v_add_f32_e32 v111, v31, v103
	global_store_dwordx2 v244, v[110:111], s[26:27] offset:128 nt
	s_endpgm
